# v69 + P0 silu(c) fill: 32 loads issued before the (now unrolled) fill loop
# speedup vs baseline: 1.0075x; 1.0075x over previous
; __device__ __forceinline__ void ph0_adaln(const Args& a, LAS unsigned char* lds, int tid, int G, int bid) {
;     ...
;     for (int ub = bid; ub < MODW / 64; ub += G) {
;         if (!have) { for (int i = tid; i < NB * DM; i += NTHR) { const int b = i >> 11, k = i & 2047; const float v = c[i]; cond[k * 8 + b] = v / (1.0f + expf(-v)); } __syncthreads(); have = true; }
.LBB0_23:
	s_and_b64 vcc, exec, s[2:3]
	v_writelane_b32 v250, s20, 60
	s_cbranch_vccnz .LBB0_32
	s_load_dwordx16 s[12:27], s[34:35], 0x0
	s_mov_b64 s[8:9], 0
	v_mov_b32_e32 v4, 16
	v_mov_b64_e32 v[2:3], v[0:1]
	s_mov_b32 s10, 0xbfb8aa3b
	s_waitcnt lgkmcnt(0)
	v_lshlrev_b32_e32 v78, 2, v0
	v_add_u32_e32 v79, 0x1000, v78
	s_mov_b64 s[98:99], s[14:15]
	global_load_dword v46, v78, s[98:99]
	global_load_dword v47, v79, s[98:99] offset:2048
	global_load_dword v48, v78, s[98:99] offset:2048
	global_load_dword v49, v79, s[98:99]
	s_add_u32 s98, s98, 0x2000
	s_addc_u32 s99, s99, 0
	global_load_dword v50, v78, s[98:99]
	global_load_dword v51, v79, s[98:99] offset:2048
	global_load_dword v52, v78, s[98:99] offset:2048
	global_load_dword v53, v79, s[98:99]
	s_add_u32 s98, s98, 0x2000
	s_addc_u32 s99, s99, 0
	global_load_dword v54, v78, s[98:99]
	global_load_dword v55, v79, s[98:99] offset:2048
	global_load_dword v56, v78, s[98:99] offset:2048
	global_load_dword v57, v79, s[98:99]
	s_add_u32 s98, s98, 0x2000
	s_addc_u32 s99, s99, 0
	global_load_dword v58, v78, s[98:99]
	global_load_dword v59, v79, s[98:99] offset:2048
	global_load_dword v60, v78, s[98:99] offset:2048
	global_load_dword v61, v79, s[98:99]
	s_add_u32 s98, s98, 0x2000
	s_addc_u32 s99, s99, 0
	global_load_dword v62, v78, s[98:99]
	global_load_dword v63, v79, s[98:99] offset:2048
	global_load_dword v64, v78, s[98:99] offset:2048
	global_load_dword v65, v79, s[98:99]
	s_add_u32 s98, s98, 0x2000
	s_addc_u32 s99, s99, 0
	global_load_dword v66, v78, s[98:99]
	global_load_dword v67, v79, s[98:99] offset:2048
	global_load_dword v68, v78, s[98:99] offset:2048
	global_load_dword v69, v79, s[98:99]
	s_add_u32 s98, s98, 0x2000
	s_addc_u32 s99, s99, 0
	global_load_dword v70, v78, s[98:99]
	global_load_dword v71, v79, s[98:99] offset:2048
	global_load_dword v72, v78, s[98:99] offset:2048
	global_load_dword v73, v79, s[98:99]
	s_add_u32 s98, s98, 0x2000
	s_addc_u32 s99, s99, 0
	global_load_dword v74, v78, s[98:99]
	global_load_dword v75, v79, s[98:99] offset:2048
	global_load_dword v76, v78, s[98:99] offset:2048
	global_load_dword v77, v79, s[98:99]
.LBB0_25:
	v_mov_b32_e32 v34, v2
	v_lshlrev_b32_e32 v10, 3, v2
	v_lshrrev_b32_e32 v11, 9, v2
	v_add_u32_e32 v6, 0x400, v3
	v_mov_b32_e32 v7, v35
	s_waitcnt lgkmcnt(0)
	v_lshl_add_u64 v[8:9], v[34:35], 2, s[14:15]
	v_mov_b32_e32 v34, v3
	v_and_b32_e32 v13, 0x3ff8, v10
	v_and_b32_e32 v14, 0x7ffffc, v11
	v_lshl_add_u64 v[10:11], v[6:7], 2, s[14:15]
	v_lshlrev_b32_e32 v15, 3, v6
	v_lshrrev_b32_e32 v16, 9, v6
	v_lshl_add_u64 v[6:7], v[34:35], 2, s[14:15]
	v_add_u32_e32 v34, 0x400, v2
	v_lshlrev_b32_e32 v13, 2, v13
	s_nop 0
	s_nop 0
	v_lshl_add_u64 v[6:7], v[34:35], 2, s[14:15]
	v_add3_u32 v13, 0, v13, v14
	v_lshlrev_b32_e32 v5, 3, v3
	v_lshrrev_b32_e32 v12, 9, v3
	v_and_b32_e32 v5, 0x3ff8, v5
	v_and_b32_e32 v12, 0x7ffffc, v12
	v_lshlrev_b32_e32 v5, 2, v5
	v_lshlrev_b32_e32 v8, 3, v34
	v_add3_u32 v5, 0, v5, v12
	v_lshrrev_b32_e32 v12, 9, v34
	v_and_b32_e32 v6, 0x3ff8, v8
	v_and_b32_e32 v15, 0x3ff8, v15
	v_and_b32_e32 v7, 0x7ffffc, v12
	v_lshlrev_b32_e32 v6, 2, v6
	v_and_b32_e32 v16, 0x7ffffc, v16
	v_lshlrev_b32_e32 v9, 2, v15
	v_add3_u32 v15, 0, v6, v7
	v_add3_u32 v12, 0, v9, v16
	v_add_u32_e32 v4, -2, v4
	v_cmp_eq_u32_e32 vcc, 0, v4
	s_or_b64 s[8:9], vcc, s[8:9]
	v_add_u32_e32 v3, 0x800, v3
	v_add_u32_e32 v2, 0x800, v2
	s_waitcnt vmcnt(28)
	v_mov_b32_e32 v17, v46
	v_mov_b32_e32 v10, v47
	v_mov_b32_e32 v11, v48
	v_mov_b32_e32 v14, v49
	v_mul_f32_e32 v6, 0xbfb8aa3b, v17
	v_mul_f32_e32 v7, 0xbfb8aa3b, v10
	v_mul_f32_e32 v8, 0xbfb8aa3b, v11
	v_fma_f32 v9, v17, s10, -v6
	v_rndne_f32_e32 v16, v6
	v_fma_f32 v18, v10, s10, -v7
	v_rndne_f32_e32 v19, v7
	v_fma_f32 v20, v11, s10, -v8
	v_rndne_f32_e32 v21, v8
	v_fmac_f32_e32 v9, 0xb2a5705f, v17
	v_sub_f32_e32 v6, v6, v16
	v_mul_f32_e32 v22, 0xbfb8aa3b, v14
	v_fmac_f32_e32 v18, 0xb2a5705f, v10
	v_sub_f32_e32 v7, v7, v19
	v_fmac_f32_e32 v20, 0xb2a5705f, v11
	v_sub_f32_e32 v8, v8, v21
	v_add_f32_e32 v6, v6, v9
	v_fma_f32 v9, v14, s10, -v22
	v_rndne_f32_e32 v23, v22
	v_add_f32_e32 v7, v7, v18
	v_cvt_i32_f32_e32 v19, v19
	v_add_f32_e32 v8, v8, v20
	v_fmac_f32_e32 v9, 0xb2a5705f, v14
	v_sub_f32_e32 v18, v22, v23
	v_exp_f32_e32 v7, v7
	v_cvt_i32_f32_e32 v16, v16
	v_cvt_i32_f32_e32 v21, v21
	v_exp_f32_e32 v6, v6
	v_exp_f32_e32 v8, v8
	v_add_f32_e32 v9, v18, v9
	v_cvt_i32_f32_e32 v20, v23
	v_exp_f32_e32 v9, v9
	v_ldexp_f32 v7, v7, v19
	v_cmp_nlt_f32_e64 s[2:3], s33, v10
	v_ldexp_f32 v6, v6, v16
	v_cmp_nlt_f32_e32 vcc, s33, v17
	v_ldexp_f32 v8, v8, v21
	v_cndmask_b32_e64 v7, 0, v7, s[2:3]
	v_cmp_ngt_f32_e64 s[2:3], s1, v10
	v_cmp_nlt_f32_e64 s[4:5], s33, v11
	v_cndmask_b32_e32 v6, 0, v6, vcc
	v_cmp_ngt_f32_e32 vcc, s1, v17
	v_cndmask_b32_e64 v8, 0, v8, s[4:5]
	v_ldexp_f32 v16, v9, v20
	v_cndmask_b32_e64 v9, v152, v7, s[2:3]
	v_cmp_ngt_f32_e64 s[2:3], s1, v11
	v_cndmask_b32_e32 v6, v152, v6, vcc
	v_cmp_nlt_f32_e32 vcc, s33, v14
	v_cndmask_b32_e64 v7, v152, v8, s[2:3]
	v_pk_add_f32 v[6:7], v[6:7], 1.0 op_sel_hi:[1,0]
	v_cndmask_b32_e32 v8, 0, v16, vcc
	v_cmp_ngt_f32_e32 vcc, s1, v14
	v_div_scale_f32 v16, s[2:3], v7, v7, v11
	s_nop 0
	v_cndmask_b32_e32 v8, v152, v8, vcc
	v_div_scale_f32 v19, s[2:3], v6, v6, v17
	v_pk_add_f32 v[8:9], v[8:9], 1.0 op_sel_hi:[1,0]
	v_rcp_f32_e32 v21, v16
	v_rcp_f32_e32 v22, v19
	v_div_scale_f32 v23, s[4:5], v9, v9, v10
	v_div_scale_f32 v25, s[6:7], v8, v8, v14
	v_rcp_f32_e32 v27, v23
	v_rcp_f32_e32 v28, v25
	v_fma_f32 v29, -v16, v21, 1.0
	v_div_scale_f32 v18, vcc, v11, v7, v11
	v_fma_f32 v30, -v19, v22, 1.0
	v_fmac_f32_e32 v21, v29, v21
	v_div_scale_f32 v20, s[2:3], v17, v6, v17
	v_fmac_f32_e32 v22, v30, v22
	v_fma_f32 v29, -v23, v27, 1.0
	v_mul_f32_e32 v31, v18, v21
	v_div_scale_f32 v24, s[4:5], v10, v9, v10
	v_fma_f32 v30, -v25, v28, 1.0
	v_mul_f32_e32 v32, v20, v22
	v_fmac_f32_e32 v27, v29, v27
	v_fma_f32 v29, -v16, v31, v18
	v_div_scale_f32 v26, s[6:7], v14, v8, v14
	v_fmac_f32_e32 v28, v30, v28
	v_fma_f32 v30, -v19, v32, v20
	v_mul_f32_e32 v33, v24, v27
	v_fmac_f32_e32 v31, v29, v21
	v_mul_f32_e32 v34, v26, v28
	v_fmac_f32_e32 v32, v30, v22
	v_fma_f32 v29, -v23, v33, v24
	v_fma_f32 v16, -v16, v31, v18
	v_fma_f32 v30, -v25, v34, v26
	v_fma_f32 v18, -v19, v32, v20
	v_fmac_f32_e32 v33, v29, v27
	v_div_fmas_f32 v16, v16, v21, v31
	s_mov_b64 vcc, s[2:3]
	v_fmac_f32_e32 v34, v30, v28
	v_fma_f32 v19, -v23, v33, v24
	v_div_fixup_f32 v7, v16, v7, v11
	v_div_fmas_f32 v11, v18, v22, v32
	s_mov_b64 vcc, s[4:5]
	v_fma_f32 v20, -v25, v34, v26
	v_div_fixup_f32 v6, v11, v6, v17
	v_div_fmas_f32 v11, v19, v27, v33
	s_mov_b64 vcc, s[6:7]
	ds_write_b32 v13, v6
	ds_write_b32 v5, v7
	v_div_fmas_f32 v6, v20, v28, v34
	v_div_fixup_f32 v6, v6, v8, v14
	v_div_fixup_f32 v5, v11, v9, v10
	ds_write_b32 v15, v6
	ds_write_b32 v12, v5
	v_mov_b32_e32 v34, v2
	v_lshlrev_b32_e32 v10, 3, v2
	v_lshrrev_b32_e32 v11, 9, v2
	v_add_u32_e32 v6, 0x400, v3
	v_mov_b32_e32 v7, v35
	s_waitcnt lgkmcnt(0)
; __device__ __forceinline__ void ph0_adaln(const Args& a, LAS unsigned char* lds, int tid, int G, int bid) {
;     ...
;     for (int ub = bid; ub < MODW / 64; ub += G) {
;         if (!have) { for (int i = tid; i < NB * DM; i += NTHR) { const int b = i >> 11, k = i & 2047; const float v = c[i]; cond[k * 8 + b] = v / (1.0f + expf(-v)); } __syncthreads(); have = true; }
	v_lshl_add_u64 v[8:9], v[34:35], 2, s[14:15]
	v_mov_b32_e32 v34, v3
	v_and_b32_e32 v13, 0x3ff8, v10
	v_and_b32_e32 v14, 0x7ffffc, v11
	v_lshl_add_u64 v[10:11], v[6:7], 2, s[14:15]
	v_lshlrev_b32_e32 v15, 3, v6
	v_lshrrev_b32_e32 v16, 9, v6
	v_lshl_add_u64 v[6:7], v[34:35], 2, s[14:15]
	v_add_u32_e32 v34, 0x400, v2
	v_lshlrev_b32_e32 v13, 2, v13
	s_nop 0
	s_nop 0
	v_lshl_add_u64 v[6:7], v[34:35], 2, s[14:15]
	v_add3_u32 v13, 0, v13, v14
	v_lshlrev_b32_e32 v5, 3, v3
	v_lshrrev_b32_e32 v12, 9, v3
	v_and_b32_e32 v5, 0x3ff8, v5
	v_and_b32_e32 v12, 0x7ffffc, v12
	v_lshlrev_b32_e32 v5, 2, v5
	v_lshlrev_b32_e32 v8, 3, v34
	v_add3_u32 v5, 0, v5, v12
	v_lshrrev_b32_e32 v12, 9, v34
	v_and_b32_e32 v6, 0x3ff8, v8
	v_and_b32_e32 v15, 0x3ff8, v15
	v_and_b32_e32 v7, 0x7ffffc, v12
	v_lshlrev_b32_e32 v6, 2, v6
	v_and_b32_e32 v16, 0x7ffffc, v16
	v_lshlrev_b32_e32 v9, 2, v15
	v_add3_u32 v15, 0, v6, v7
	v_add3_u32 v12, 0, v9, v16
	v_add_u32_e32 v4, -2, v4
	v_cmp_eq_u32_e32 vcc, 0, v4
	s_or_b64 s[8:9], vcc, s[8:9]
	v_add_u32_e32 v3, 0x800, v3
	v_add_u32_e32 v2, 0x800, v2
	s_waitcnt vmcnt(24)
	v_mov_b32_e32 v17, v50
	v_mov_b32_e32 v10, v51
	v_mov_b32_e32 v11, v52
	v_mov_b32_e32 v14, v53
	v_mul_f32_e32 v6, 0xbfb8aa3b, v17
	v_mul_f32_e32 v7, 0xbfb8aa3b, v10
	v_mul_f32_e32 v8, 0xbfb8aa3b, v11
	v_fma_f32 v9, v17, s10, -v6
	v_rndne_f32_e32 v16, v6
	v_fma_f32 v18, v10, s10, -v7
	v_rndne_f32_e32 v19, v7
	v_fma_f32 v20, v11, s10, -v8
	v_rndne_f32_e32 v21, v8
	v_fmac_f32_e32 v9, 0xb2a5705f, v17
	v_sub_f32_e32 v6, v6, v16
	v_mul_f32_e32 v22, 0xbfb8aa3b, v14
	v_fmac_f32_e32 v18, 0xb2a5705f, v10
	v_sub_f32_e32 v7, v7, v19
	v_fmac_f32_e32 v20, 0xb2a5705f, v11
	v_sub_f32_e32 v8, v8, v21
	v_add_f32_e32 v6, v6, v9
	v_fma_f32 v9, v14, s10, -v22
	v_rndne_f32_e32 v23, v22
	v_add_f32_e32 v7, v7, v18
	v_cvt_i32_f32_e32 v19, v19
	v_add_f32_e32 v8, v8, v20
	v_fmac_f32_e32 v9, 0xb2a5705f, v14
	v_sub_f32_e32 v18, v22, v23
	v_exp_f32_e32 v7, v7
	v_cvt_i32_f32_e32 v16, v16
	v_cvt_i32_f32_e32 v21, v21
	v_exp_f32_e32 v6, v6
	v_exp_f32_e32 v8, v8
	v_add_f32_e32 v9, v18, v9
	v_cvt_i32_f32_e32 v20, v23
	v_exp_f32_e32 v9, v9
	v_ldexp_f32 v7, v7, v19
	v_cmp_nlt_f32_e64 s[2:3], s33, v10
	v_ldexp_f32 v6, v6, v16
	v_cmp_nlt_f32_e32 vcc, s33, v17
	v_ldexp_f32 v8, v8, v21
	v_cndmask_b32_e64 v7, 0, v7, s[2:3]
	v_cmp_ngt_f32_e64 s[2:3], s1, v10
	v_cmp_nlt_f32_e64 s[4:5], s33, v11
	v_cndmask_b32_e32 v6, 0, v6, vcc
	v_cmp_ngt_f32_e32 vcc, s1, v17
	v_cndmask_b32_e64 v8, 0, v8, s[4:5]
	v_ldexp_f32 v16, v9, v20
	v_cndmask_b32_e64 v9, v152, v7, s[2:3]
	v_cmp_ngt_f32_e64 s[2:3], s1, v11
	v_cndmask_b32_e32 v6, v152, v6, vcc
	v_cmp_nlt_f32_e32 vcc, s33, v14
	v_cndmask_b32_e64 v7, v152, v8, s[2:3]
	v_pk_add_f32 v[6:7], v[6:7], 1.0 op_sel_hi:[1,0]
	v_cndmask_b32_e32 v8, 0, v16, vcc
	v_cmp_ngt_f32_e32 vcc, s1, v14
	v_div_scale_f32 v16, s[2:3], v7, v7, v11
	s_nop 0
	v_cndmask_b32_e32 v8, v152, v8, vcc
	v_div_scale_f32 v19, s[2:3], v6, v6, v17
	v_pk_add_f32 v[8:9], v[8:9], 1.0 op_sel_hi:[1,0]
	v_rcp_f32_e32 v21, v16
	v_rcp_f32_e32 v22, v19
	v_div_scale_f32 v23, s[4:5], v9, v9, v10
	v_div_scale_f32 v25, s[6:7], v8, v8, v14
	v_rcp_f32_e32 v27, v23
	v_rcp_f32_e32 v28, v25
	v_fma_f32 v29, -v16, v21, 1.0
	v_div_scale_f32 v18, vcc, v11, v7, v11
	v_fma_f32 v30, -v19, v22, 1.0
	v_fmac_f32_e32 v21, v29, v21
	v_div_scale_f32 v20, s[2:3], v17, v6, v17
	v_fmac_f32_e32 v22, v30, v22
	v_fma_f32 v29, -v23, v27, 1.0
	v_mul_f32_e32 v31, v18, v21
	v_div_scale_f32 v24, s[4:5], v10, v9, v10
	v_fma_f32 v30, -v25, v28, 1.0
	v_mul_f32_e32 v32, v20, v22
	v_fmac_f32_e32 v27, v29, v27
	v_fma_f32 v29, -v16, v31, v18
	v_div_scale_f32 v26, s[6:7], v14, v8, v14
	v_fmac_f32_e32 v28, v30, v28
	v_fma_f32 v30, -v19, v32, v20
	v_mul_f32_e32 v33, v24, v27
	v_fmac_f32_e32 v31, v29, v21
	v_mul_f32_e32 v34, v26, v28
	v_fmac_f32_e32 v32, v30, v22
	v_fma_f32 v29, -v23, v33, v24
	v_fma_f32 v16, -v16, v31, v18
	v_fma_f32 v30, -v25, v34, v26
	v_fma_f32 v18, -v19, v32, v20
	v_fmac_f32_e32 v33, v29, v27
	v_div_fmas_f32 v16, v16, v21, v31
	s_mov_b64 vcc, s[2:3]
	v_fmac_f32_e32 v34, v30, v28
	v_fma_f32 v19, -v23, v33, v24
	v_div_fixup_f32 v7, v16, v7, v11
	v_div_fmas_f32 v11, v18, v22, v32
	s_mov_b64 vcc, s[4:5]
	v_fma_f32 v20, -v25, v34, v26
	v_div_fixup_f32 v6, v11, v6, v17
	v_div_fmas_f32 v11, v19, v27, v33
	s_mov_b64 vcc, s[6:7]
	ds_write_b32 v13, v6
	ds_write_b32 v5, v7
	v_div_fmas_f32 v6, v20, v28, v34
	v_div_fixup_f32 v6, v6, v8, v14
	v_div_fixup_f32 v5, v11, v9, v10
	ds_write_b32 v15, v6
	ds_write_b32 v12, v5
	v_mov_b32_e32 v34, v2
	v_lshlrev_b32_e32 v10, 3, v2
	v_lshrrev_b32_e32 v11, 9, v2
	v_add_u32_e32 v6, 0x400, v3
	v_mov_b32_e32 v7, v35
	s_waitcnt lgkmcnt(0)
	v_lshl_add_u64 v[8:9], v[34:35], 2, s[14:15]
	v_mov_b32_e32 v34, v3
	v_and_b32_e32 v13, 0x3ff8, v10
	v_and_b32_e32 v14, 0x7ffffc, v11
	v_lshl_add_u64 v[10:11], v[6:7], 2, s[14:15]
	v_lshlrev_b32_e32 v15, 3, v6
	v_lshrrev_b32_e32 v16, 9, v6
	v_lshl_add_u64 v[6:7], v[34:35], 2, s[14:15]
	v_add_u32_e32 v34, 0x400, v2
	v_lshlrev_b32_e32 v13, 2, v13
	s_nop 0
	s_nop 0
	v_lshl_add_u64 v[6:7], v[34:35], 2, s[14:15]
	v_add3_u32 v13, 0, v13, v14
	v_lshlrev_b32_e32 v5, 3, v3
	v_lshrrev_b32_e32 v12, 9, v3
	v_and_b32_e32 v5, 0x3ff8, v5
	v_and_b32_e32 v12, 0x7ffffc, v12
	v_lshlrev_b32_e32 v5, 2, v5
	v_lshlrev_b32_e32 v8, 3, v34
	v_add3_u32 v5, 0, v5, v12
	v_lshrrev_b32_e32 v12, 9, v34
	v_and_b32_e32 v6, 0x3ff8, v8
	v_and_b32_e32 v15, 0x3ff8, v15
	v_and_b32_e32 v7, 0x7ffffc, v12
	v_lshlrev_b32_e32 v6, 2, v6
	v_and_b32_e32 v16, 0x7ffffc, v16
	v_lshlrev_b32_e32 v9, 2, v15
	v_add3_u32 v15, 0, v6, v7
	v_add3_u32 v12, 0, v9, v16
	v_add_u32_e32 v4, -2, v4
	v_cmp_eq_u32_e32 vcc, 0, v4
	s_or_b64 s[8:9], vcc, s[8:9]
	v_add_u32_e32 v3, 0x800, v3
	v_add_u32_e32 v2, 0x800, v2
	s_waitcnt vmcnt(20)
; __device__ __forceinline__ void ph0_adaln(const Args& a, LAS unsigned char* lds, int tid, int G, int bid) {
;     ...
;     for (int ub = bid; ub < MODW / 64; ub += G) {
;         if (!have) { for (int i = tid; i < NB * DM; i += NTHR) { const int b = i >> 11, k = i & 2047; const float v = c[i]; cond[k * 8 + b] = v / (1.0f + expf(-v)); } __syncthreads(); have = true; }
	v_mov_b32_e32 v17, v54
	v_mov_b32_e32 v10, v55
	v_mov_b32_e32 v11, v56
	v_mov_b32_e32 v14, v57
	v_mul_f32_e32 v6, 0xbfb8aa3b, v17
	v_mul_f32_e32 v7, 0xbfb8aa3b, v10
	v_mul_f32_e32 v8, 0xbfb8aa3b, v11
	v_fma_f32 v9, v17, s10, -v6
	v_rndne_f32_e32 v16, v6
	v_fma_f32 v18, v10, s10, -v7
	v_rndne_f32_e32 v19, v7
	v_fma_f32 v20, v11, s10, -v8
	v_rndne_f32_e32 v21, v8
	v_fmac_f32_e32 v9, 0xb2a5705f, v17
	v_sub_f32_e32 v6, v6, v16
	v_mul_f32_e32 v22, 0xbfb8aa3b, v14
	v_fmac_f32_e32 v18, 0xb2a5705f, v10
	v_sub_f32_e32 v7, v7, v19
	v_fmac_f32_e32 v20, 0xb2a5705f, v11
	v_sub_f32_e32 v8, v8, v21
	v_add_f32_e32 v6, v6, v9
	v_fma_f32 v9, v14, s10, -v22
	v_rndne_f32_e32 v23, v22
	v_add_f32_e32 v7, v7, v18
	v_cvt_i32_f32_e32 v19, v19
	v_add_f32_e32 v8, v8, v20
	v_fmac_f32_e32 v9, 0xb2a5705f, v14
	v_sub_f32_e32 v18, v22, v23
	v_exp_f32_e32 v7, v7
	v_cvt_i32_f32_e32 v16, v16
	v_cvt_i32_f32_e32 v21, v21
	v_exp_f32_e32 v6, v6
	v_exp_f32_e32 v8, v8
	v_add_f32_e32 v9, v18, v9
	v_cvt_i32_f32_e32 v20, v23
	v_exp_f32_e32 v9, v9
	v_ldexp_f32 v7, v7, v19
	v_cmp_nlt_f32_e64 s[2:3], s33, v10
	v_ldexp_f32 v6, v6, v16
	v_cmp_nlt_f32_e32 vcc, s33, v17
	v_ldexp_f32 v8, v8, v21
	v_cndmask_b32_e64 v7, 0, v7, s[2:3]
	v_cmp_ngt_f32_e64 s[2:3], s1, v10
	v_cmp_nlt_f32_e64 s[4:5], s33, v11
	v_cndmask_b32_e32 v6, 0, v6, vcc
	v_cmp_ngt_f32_e32 vcc, s1, v17
	v_cndmask_b32_e64 v8, 0, v8, s[4:5]
	v_ldexp_f32 v16, v9, v20
	v_cndmask_b32_e64 v9, v152, v7, s[2:3]
	v_cmp_ngt_f32_e64 s[2:3], s1, v11
	v_cndmask_b32_e32 v6, v152, v6, vcc
	v_cmp_nlt_f32_e32 vcc, s33, v14
	v_cndmask_b32_e64 v7, v152, v8, s[2:3]
	v_pk_add_f32 v[6:7], v[6:7], 1.0 op_sel_hi:[1,0]
	v_cndmask_b32_e32 v8, 0, v16, vcc
	v_cmp_ngt_f32_e32 vcc, s1, v14
	v_div_scale_f32 v16, s[2:3], v7, v7, v11
	s_nop 0
	v_cndmask_b32_e32 v8, v152, v8, vcc
	v_div_scale_f32 v19, s[2:3], v6, v6, v17
	v_pk_add_f32 v[8:9], v[8:9], 1.0 op_sel_hi:[1,0]
	v_rcp_f32_e32 v21, v16
	v_rcp_f32_e32 v22, v19
	v_div_scale_f32 v23, s[4:5], v9, v9, v10
	v_div_scale_f32 v25, s[6:7], v8, v8, v14
	v_rcp_f32_e32 v27, v23
	v_rcp_f32_e32 v28, v25
	v_fma_f32 v29, -v16, v21, 1.0
	v_div_scale_f32 v18, vcc, v11, v7, v11
	v_fma_f32 v30, -v19, v22, 1.0
	v_fmac_f32_e32 v21, v29, v21
	v_div_scale_f32 v20, s[2:3], v17, v6, v17
	v_fmac_f32_e32 v22, v30, v22
	v_fma_f32 v29, -v23, v27, 1.0
	v_mul_f32_e32 v31, v18, v21
	v_div_scale_f32 v24, s[4:5], v10, v9, v10
	v_fma_f32 v30, -v25, v28, 1.0
	v_mul_f32_e32 v32, v20, v22
	v_fmac_f32_e32 v27, v29, v27
	v_fma_f32 v29, -v16, v31, v18
	v_div_scale_f32 v26, s[6:7], v14, v8, v14
	v_fmac_f32_e32 v28, v30, v28
	v_fma_f32 v30, -v19, v32, v20
	v_mul_f32_e32 v33, v24, v27
	v_fmac_f32_e32 v31, v29, v21
	v_mul_f32_e32 v34, v26, v28
	v_fmac_f32_e32 v32, v30, v22
	v_fma_f32 v29, -v23, v33, v24
	v_fma_f32 v16, -v16, v31, v18
	v_fma_f32 v30, -v25, v34, v26
	v_fma_f32 v18, -v19, v32, v20
	v_fmac_f32_e32 v33, v29, v27
	v_div_fmas_f32 v16, v16, v21, v31
	s_mov_b64 vcc, s[2:3]
	v_fmac_f32_e32 v34, v30, v28
	v_fma_f32 v19, -v23, v33, v24
	v_div_fixup_f32 v7, v16, v7, v11
	v_div_fmas_f32 v11, v18, v22, v32
	s_mov_b64 vcc, s[4:5]
	v_fma_f32 v20, -v25, v34, v26
	v_div_fixup_f32 v6, v11, v6, v17
	v_div_fmas_f32 v11, v19, v27, v33
	s_mov_b64 vcc, s[6:7]
	ds_write_b32 v13, v6
	ds_write_b32 v5, v7
	v_div_fmas_f32 v6, v20, v28, v34
	v_div_fixup_f32 v6, v6, v8, v14
	v_div_fixup_f32 v5, v11, v9, v10
	ds_write_b32 v15, v6
	ds_write_b32 v12, v5
	v_mov_b32_e32 v34, v2
	v_lshlrev_b32_e32 v10, 3, v2
	v_lshrrev_b32_e32 v11, 9, v2
	v_add_u32_e32 v6, 0x400, v3
	v_mov_b32_e32 v7, v35
	s_waitcnt lgkmcnt(0)
	v_lshl_add_u64 v[8:9], v[34:35], 2, s[14:15]
	v_mov_b32_e32 v34, v3
	v_and_b32_e32 v13, 0x3ff8, v10
	v_and_b32_e32 v14, 0x7ffffc, v11
	v_lshl_add_u64 v[10:11], v[6:7], 2, s[14:15]
	v_lshlrev_b32_e32 v15, 3, v6
	v_lshrrev_b32_e32 v16, 9, v6
	v_lshl_add_u64 v[6:7], v[34:35], 2, s[14:15]
	v_add_u32_e32 v34, 0x400, v2
	v_lshlrev_b32_e32 v13, 2, v13
	s_nop 0
	s_nop 0
	v_lshl_add_u64 v[6:7], v[34:35], 2, s[14:15]
	v_add3_u32 v13, 0, v13, v14
	v_lshlrev_b32_e32 v5, 3, v3
	v_lshrrev_b32_e32 v12, 9, v3
	v_and_b32_e32 v5, 0x3ff8, v5
	v_and_b32_e32 v12, 0x7ffffc, v12
	v_lshlrev_b32_e32 v5, 2, v5
	v_lshlrev_b32_e32 v8, 3, v34
	v_add3_u32 v5, 0, v5, v12
	v_lshrrev_b32_e32 v12, 9, v34
	v_and_b32_e32 v6, 0x3ff8, v8
	v_and_b32_e32 v15, 0x3ff8, v15
	v_and_b32_e32 v7, 0x7ffffc, v12
	v_lshlrev_b32_e32 v6, 2, v6
	v_and_b32_e32 v16, 0x7ffffc, v16
	v_lshlrev_b32_e32 v9, 2, v15
	v_add3_u32 v15, 0, v6, v7
	v_add3_u32 v12, 0, v9, v16
	v_add_u32_e32 v4, -2, v4
	v_cmp_eq_u32_e32 vcc, 0, v4
	s_or_b64 s[8:9], vcc, s[8:9]
	v_add_u32_e32 v3, 0x800, v3
	v_add_u32_e32 v2, 0x800, v2
	s_waitcnt vmcnt(16)
; __device__ __forceinline__ void ph0_adaln(const Args& a, LAS unsigned char* lds, int tid, int G, int bid) {
;     ...
;     for (int ub = bid; ub < MODW / 64; ub += G) {
;         if (!have) { for (int i = tid; i < NB * DM; i += NTHR) { const int b = i >> 11, k = i & 2047; const float v = c[i]; cond[k * 8 + b] = v / (1.0f + expf(-v)); } __syncthreads(); have = true; }
	v_mov_b32_e32 v17, v58
	v_mov_b32_e32 v10, v59
	v_mov_b32_e32 v11, v60
	v_mov_b32_e32 v14, v61
	v_mul_f32_e32 v6, 0xbfb8aa3b, v17
	v_mul_f32_e32 v7, 0xbfb8aa3b, v10
	v_mul_f32_e32 v8, 0xbfb8aa3b, v11
	v_fma_f32 v9, v17, s10, -v6
	v_rndne_f32_e32 v16, v6
	v_fma_f32 v18, v10, s10, -v7
	v_rndne_f32_e32 v19, v7
	v_fma_f32 v20, v11, s10, -v8
	v_rndne_f32_e32 v21, v8
	v_fmac_f32_e32 v9, 0xb2a5705f, v17
	v_sub_f32_e32 v6, v6, v16
	v_mul_f32_e32 v22, 0xbfb8aa3b, v14
	v_fmac_f32_e32 v18, 0xb2a5705f, v10
	v_sub_f32_e32 v7, v7, v19
	v_fmac_f32_e32 v20, 0xb2a5705f, v11
	v_sub_f32_e32 v8, v8, v21
	v_add_f32_e32 v6, v6, v9
	v_fma_f32 v9, v14, s10, -v22
	v_rndne_f32_e32 v23, v22
	v_add_f32_e32 v7, v7, v18
	v_cvt_i32_f32_e32 v19, v19
	v_add_f32_e32 v8, v8, v20
	v_fmac_f32_e32 v9, 0xb2a5705f, v14
	v_sub_f32_e32 v18, v22, v23
	v_exp_f32_e32 v7, v7
	v_cvt_i32_f32_e32 v16, v16
	v_cvt_i32_f32_e32 v21, v21
	v_exp_f32_e32 v6, v6
	v_exp_f32_e32 v8, v8
	v_add_f32_e32 v9, v18, v9
	v_cvt_i32_f32_e32 v20, v23
	v_exp_f32_e32 v9, v9
	v_ldexp_f32 v7, v7, v19
	v_cmp_nlt_f32_e64 s[2:3], s33, v10
	v_ldexp_f32 v6, v6, v16
	v_cmp_nlt_f32_e32 vcc, s33, v17
	v_ldexp_f32 v8, v8, v21
	v_cndmask_b32_e64 v7, 0, v7, s[2:3]
	v_cmp_ngt_f32_e64 s[2:3], s1, v10
	v_cmp_nlt_f32_e64 s[4:5], s33, v11
	v_cndmask_b32_e32 v6, 0, v6, vcc
	v_cmp_ngt_f32_e32 vcc, s1, v17
	v_cndmask_b32_e64 v8, 0, v8, s[4:5]
	v_ldexp_f32 v16, v9, v20
	v_cndmask_b32_e64 v9, v152, v7, s[2:3]
	v_cmp_ngt_f32_e64 s[2:3], s1, v11
	v_cndmask_b32_e32 v6, v152, v6, vcc
	v_cmp_nlt_f32_e32 vcc, s33, v14
	v_cndmask_b32_e64 v7, v152, v8, s[2:3]
	v_pk_add_f32 v[6:7], v[6:7], 1.0 op_sel_hi:[1,0]
	v_cndmask_b32_e32 v8, 0, v16, vcc
	v_cmp_ngt_f32_e32 vcc, s1, v14
	v_div_scale_f32 v16, s[2:3], v7, v7, v11
	s_nop 0
	v_cndmask_b32_e32 v8, v152, v8, vcc
	v_div_scale_f32 v19, s[2:3], v6, v6, v17
	v_pk_add_f32 v[8:9], v[8:9], 1.0 op_sel_hi:[1,0]
	v_rcp_f32_e32 v21, v16
	v_rcp_f32_e32 v22, v19
	v_div_scale_f32 v23, s[4:5], v9, v9, v10
	v_div_scale_f32 v25, s[6:7], v8, v8, v14
	v_rcp_f32_e32 v27, v23
	v_rcp_f32_e32 v28, v25
	v_fma_f32 v29, -v16, v21, 1.0
	v_div_scale_f32 v18, vcc, v11, v7, v11
	v_fma_f32 v30, -v19, v22, 1.0
	v_fmac_f32_e32 v21, v29, v21
	v_div_scale_f32 v20, s[2:3], v17, v6, v17
	v_fmac_f32_e32 v22, v30, v22
	v_fma_f32 v29, -v23, v27, 1.0
	v_mul_f32_e32 v31, v18, v21
	v_div_scale_f32 v24, s[4:5], v10, v9, v10
	v_fma_f32 v30, -v25, v28, 1.0
	v_mul_f32_e32 v32, v20, v22
	v_fmac_f32_e32 v27, v29, v27
	v_fma_f32 v29, -v16, v31, v18
	v_div_scale_f32 v26, s[6:7], v14, v8, v14
	v_fmac_f32_e32 v28, v30, v28
	v_fma_f32 v30, -v19, v32, v20
	v_mul_f32_e32 v33, v24, v27
	v_fmac_f32_e32 v31, v29, v21
	v_mul_f32_e32 v34, v26, v28
	v_fmac_f32_e32 v32, v30, v22
	v_fma_f32 v29, -v23, v33, v24
	v_fma_f32 v16, -v16, v31, v18
	v_fma_f32 v30, -v25, v34, v26
	v_fma_f32 v18, -v19, v32, v20
	v_fmac_f32_e32 v33, v29, v27
	v_div_fmas_f32 v16, v16, v21, v31
	s_mov_b64 vcc, s[2:3]
	v_fmac_f32_e32 v34, v30, v28
	v_fma_f32 v19, -v23, v33, v24
	v_div_fixup_f32 v7, v16, v7, v11
	v_div_fmas_f32 v11, v18, v22, v32
	s_mov_b64 vcc, s[4:5]
	v_fma_f32 v20, -v25, v34, v26
	v_div_fixup_f32 v6, v11, v6, v17
	v_div_fmas_f32 v11, v19, v27, v33
	s_mov_b64 vcc, s[6:7]
	ds_write_b32 v13, v6
	ds_write_b32 v5, v7
	v_div_fmas_f32 v6, v20, v28, v34
	v_div_fixup_f32 v6, v6, v8, v14
	v_div_fixup_f32 v5, v11, v9, v10
	ds_write_b32 v15, v6
	ds_write_b32 v12, v5
	v_mov_b32_e32 v34, v2
	v_lshlrev_b32_e32 v10, 3, v2
	v_lshrrev_b32_e32 v11, 9, v2
	v_add_u32_e32 v6, 0x400, v3
	v_mov_b32_e32 v7, v35
	s_waitcnt lgkmcnt(0)
	v_lshl_add_u64 v[8:9], v[34:35], 2, s[14:15]
	v_mov_b32_e32 v34, v3
	v_and_b32_e32 v13, 0x3ff8, v10
	v_and_b32_e32 v14, 0x7ffffc, v11
	v_lshl_add_u64 v[10:11], v[6:7], 2, s[14:15]
	v_lshlrev_b32_e32 v15, 3, v6
	v_lshrrev_b32_e32 v16, 9, v6
	v_lshl_add_u64 v[6:7], v[34:35], 2, s[14:15]
	v_add_u32_e32 v34, 0x400, v2
	v_lshlrev_b32_e32 v13, 2, v13
	s_nop 0
	s_nop 0
	v_lshl_add_u64 v[6:7], v[34:35], 2, s[14:15]
	v_add3_u32 v13, 0, v13, v14
	v_lshlrev_b32_e32 v5, 3, v3
	v_lshrrev_b32_e32 v12, 9, v3
	v_and_b32_e32 v5, 0x3ff8, v5
	v_and_b32_e32 v12, 0x7ffffc, v12
	v_lshlrev_b32_e32 v5, 2, v5
	v_lshlrev_b32_e32 v8, 3, v34
	v_add3_u32 v5, 0, v5, v12
	v_lshrrev_b32_e32 v12, 9, v34
	v_and_b32_e32 v6, 0x3ff8, v8
	v_and_b32_e32 v15, 0x3ff8, v15
	v_and_b32_e32 v7, 0x7ffffc, v12
	v_lshlrev_b32_e32 v6, 2, v6
	v_and_b32_e32 v16, 0x7ffffc, v16
	v_lshlrev_b32_e32 v9, 2, v15
	v_add3_u32 v15, 0, v6, v7
	v_add3_u32 v12, 0, v9, v16
	v_add_u32_e32 v4, -2, v4
	v_cmp_eq_u32_e32 vcc, 0, v4
	s_or_b64 s[8:9], vcc, s[8:9]
	v_add_u32_e32 v3, 0x800, v3
	v_add_u32_e32 v2, 0x800, v2
	s_waitcnt vmcnt(12)
; __device__ __forceinline__ void ph0_adaln(const Args& a, LAS unsigned char* lds, int tid, int G, int bid) {
;     ...
;     for (int ub = bid; ub < MODW / 64; ub += G) {
;         if (!have) { for (int i = tid; i < NB * DM; i += NTHR) { const int b = i >> 11, k = i & 2047; const float v = c[i]; cond[k * 8 + b] = v / (1.0f + expf(-v)); } __syncthreads(); have = true; }
	v_mov_b32_e32 v17, v62
	v_mov_b32_e32 v10, v63
	v_mov_b32_e32 v11, v64
	v_mov_b32_e32 v14, v65
	v_mul_f32_e32 v6, 0xbfb8aa3b, v17
	v_mul_f32_e32 v7, 0xbfb8aa3b, v10
	v_mul_f32_e32 v8, 0xbfb8aa3b, v11
	v_fma_f32 v9, v17, s10, -v6
	v_rndne_f32_e32 v16, v6
	v_fma_f32 v18, v10, s10, -v7
	v_rndne_f32_e32 v19, v7
	v_fma_f32 v20, v11, s10, -v8
	v_rndne_f32_e32 v21, v8
	v_fmac_f32_e32 v9, 0xb2a5705f, v17
	v_sub_f32_e32 v6, v6, v16
	v_mul_f32_e32 v22, 0xbfb8aa3b, v14
	v_fmac_f32_e32 v18, 0xb2a5705f, v10
	v_sub_f32_e32 v7, v7, v19
	v_fmac_f32_e32 v20, 0xb2a5705f, v11
	v_sub_f32_e32 v8, v8, v21
	v_add_f32_e32 v6, v6, v9
	v_fma_f32 v9, v14, s10, -v22
	v_rndne_f32_e32 v23, v22
	v_add_f32_e32 v7, v7, v18
	v_cvt_i32_f32_e32 v19, v19
	v_add_f32_e32 v8, v8, v20
	v_fmac_f32_e32 v9, 0xb2a5705f, v14
	v_sub_f32_e32 v18, v22, v23
	v_exp_f32_e32 v7, v7
	v_cvt_i32_f32_e32 v16, v16
	v_cvt_i32_f32_e32 v21, v21
	v_exp_f32_e32 v6, v6
	v_exp_f32_e32 v8, v8
	v_add_f32_e32 v9, v18, v9
	v_cvt_i32_f32_e32 v20, v23
	v_exp_f32_e32 v9, v9
	v_ldexp_f32 v7, v7, v19
	v_cmp_nlt_f32_e64 s[2:3], s33, v10
	v_ldexp_f32 v6, v6, v16
	v_cmp_nlt_f32_e32 vcc, s33, v17
	v_ldexp_f32 v8, v8, v21
	v_cndmask_b32_e64 v7, 0, v7, s[2:3]
	v_cmp_ngt_f32_e64 s[2:3], s1, v10
	v_cmp_nlt_f32_e64 s[4:5], s33, v11
	v_cndmask_b32_e32 v6, 0, v6, vcc
	v_cmp_ngt_f32_e32 vcc, s1, v17
	v_cndmask_b32_e64 v8, 0, v8, s[4:5]
	v_ldexp_f32 v16, v9, v20
	v_cndmask_b32_e64 v9, v152, v7, s[2:3]
	v_cmp_ngt_f32_e64 s[2:3], s1, v11
	v_cndmask_b32_e32 v6, v152, v6, vcc
	v_cmp_nlt_f32_e32 vcc, s33, v14
	v_cndmask_b32_e64 v7, v152, v8, s[2:3]
	v_pk_add_f32 v[6:7], v[6:7], 1.0 op_sel_hi:[1,0]
	v_cndmask_b32_e32 v8, 0, v16, vcc
	v_cmp_ngt_f32_e32 vcc, s1, v14
	v_div_scale_f32 v16, s[2:3], v7, v7, v11
	s_nop 0
	v_cndmask_b32_e32 v8, v152, v8, vcc
	v_div_scale_f32 v19, s[2:3], v6, v6, v17
	v_pk_add_f32 v[8:9], v[8:9], 1.0 op_sel_hi:[1,0]
	v_rcp_f32_e32 v21, v16
	v_rcp_f32_e32 v22, v19
	v_div_scale_f32 v23, s[4:5], v9, v9, v10
	v_div_scale_f32 v25, s[6:7], v8, v8, v14
	v_rcp_f32_e32 v27, v23
	v_rcp_f32_e32 v28, v25
	v_fma_f32 v29, -v16, v21, 1.0
	v_div_scale_f32 v18, vcc, v11, v7, v11
	v_fma_f32 v30, -v19, v22, 1.0
	v_fmac_f32_e32 v21, v29, v21
	v_div_scale_f32 v20, s[2:3], v17, v6, v17
	v_fmac_f32_e32 v22, v30, v22
	v_fma_f32 v29, -v23, v27, 1.0
	v_mul_f32_e32 v31, v18, v21
	v_div_scale_f32 v24, s[4:5], v10, v9, v10
	v_fma_f32 v30, -v25, v28, 1.0
	v_mul_f32_e32 v32, v20, v22
	v_fmac_f32_e32 v27, v29, v27
	v_fma_f32 v29, -v16, v31, v18
	v_div_scale_f32 v26, s[6:7], v14, v8, v14
	v_fmac_f32_e32 v28, v30, v28
	v_fma_f32 v30, -v19, v32, v20
	v_mul_f32_e32 v33, v24, v27
	v_fmac_f32_e32 v31, v29, v21
	v_mul_f32_e32 v34, v26, v28
	v_fmac_f32_e32 v32, v30, v22
	v_fma_f32 v29, -v23, v33, v24
	v_fma_f32 v16, -v16, v31, v18
	v_fma_f32 v30, -v25, v34, v26
	v_fma_f32 v18, -v19, v32, v20
	v_fmac_f32_e32 v33, v29, v27
	v_div_fmas_f32 v16, v16, v21, v31
	s_mov_b64 vcc, s[2:3]
	v_fmac_f32_e32 v34, v30, v28
	v_fma_f32 v19, -v23, v33, v24
	v_div_fixup_f32 v7, v16, v7, v11
	v_div_fmas_f32 v11, v18, v22, v32
	s_mov_b64 vcc, s[4:5]
	v_fma_f32 v20, -v25, v34, v26
	v_div_fixup_f32 v6, v11, v6, v17
	v_div_fmas_f32 v11, v19, v27, v33
	s_mov_b64 vcc, s[6:7]
	ds_write_b32 v13, v6
	ds_write_b32 v5, v7
	v_div_fmas_f32 v6, v20, v28, v34
	v_div_fixup_f32 v6, v6, v8, v14
	v_div_fixup_f32 v5, v11, v9, v10
	ds_write_b32 v15, v6
	ds_write_b32 v12, v5
	v_mov_b32_e32 v34, v2
	v_lshlrev_b32_e32 v10, 3, v2
	v_lshrrev_b32_e32 v11, 9, v2
	v_add_u32_e32 v6, 0x400, v3
	v_mov_b32_e32 v7, v35
	s_waitcnt lgkmcnt(0)
	v_lshl_add_u64 v[8:9], v[34:35], 2, s[14:15]
	v_mov_b32_e32 v34, v3
	v_and_b32_e32 v13, 0x3ff8, v10
	v_and_b32_e32 v14, 0x7ffffc, v11
	v_lshl_add_u64 v[10:11], v[6:7], 2, s[14:15]
	v_lshlrev_b32_e32 v15, 3, v6
	v_lshrrev_b32_e32 v16, 9, v6
	v_lshl_add_u64 v[6:7], v[34:35], 2, s[14:15]
	v_add_u32_e32 v34, 0x400, v2
	v_lshlrev_b32_e32 v13, 2, v13
	s_nop 0
	s_nop 0
	v_lshl_add_u64 v[6:7], v[34:35], 2, s[14:15]
	v_add3_u32 v13, 0, v13, v14
	v_lshlrev_b32_e32 v5, 3, v3
	v_lshrrev_b32_e32 v12, 9, v3
	v_and_b32_e32 v5, 0x3ff8, v5
	v_and_b32_e32 v12, 0x7ffffc, v12
	v_lshlrev_b32_e32 v5, 2, v5
	v_lshlrev_b32_e32 v8, 3, v34
	v_add3_u32 v5, 0, v5, v12
	v_lshrrev_b32_e32 v12, 9, v34
	v_and_b32_e32 v6, 0x3ff8, v8
	v_and_b32_e32 v15, 0x3ff8, v15
	v_and_b32_e32 v7, 0x7ffffc, v12
	v_lshlrev_b32_e32 v6, 2, v6
	v_and_b32_e32 v16, 0x7ffffc, v16
	v_lshlrev_b32_e32 v9, 2, v15
	v_add3_u32 v15, 0, v6, v7
	v_add3_u32 v12, 0, v9, v16
	v_add_u32_e32 v4, -2, v4
	v_cmp_eq_u32_e32 vcc, 0, v4
	s_or_b64 s[8:9], vcc, s[8:9]
	v_add_u32_e32 v3, 0x800, v3
	v_add_u32_e32 v2, 0x800, v2
	s_waitcnt vmcnt(8)
; __device__ __forceinline__ void ph0_adaln(const Args& a, LAS unsigned char* lds, int tid, int G, int bid) {
;     ...
;     for (int ub = bid; ub < MODW / 64; ub += G) {
;         if (!have) { for (int i = tid; i < NB * DM; i += NTHR) { const int b = i >> 11, k = i & 2047; const float v = c[i]; cond[k * 8 + b] = v / (1.0f + expf(-v)); } __syncthreads(); have = true; }
	v_mov_b32_e32 v17, v66
	v_mov_b32_e32 v10, v67
	v_mov_b32_e32 v11, v68
	v_mov_b32_e32 v14, v69
	v_mul_f32_e32 v6, 0xbfb8aa3b, v17
	v_mul_f32_e32 v7, 0xbfb8aa3b, v10
	v_mul_f32_e32 v8, 0xbfb8aa3b, v11
	v_fma_f32 v9, v17, s10, -v6
	v_rndne_f32_e32 v16, v6
	v_fma_f32 v18, v10, s10, -v7
	v_rndne_f32_e32 v19, v7
	v_fma_f32 v20, v11, s10, -v8
	v_rndne_f32_e32 v21, v8
	v_fmac_f32_e32 v9, 0xb2a5705f, v17
	v_sub_f32_e32 v6, v6, v16
	v_mul_f32_e32 v22, 0xbfb8aa3b, v14
	v_fmac_f32_e32 v18, 0xb2a5705f, v10
	v_sub_f32_e32 v7, v7, v19
	v_fmac_f32_e32 v20, 0xb2a5705f, v11
	v_sub_f32_e32 v8, v8, v21
	v_add_f32_e32 v6, v6, v9
	v_fma_f32 v9, v14, s10, -v22
	v_rndne_f32_e32 v23, v22
	v_add_f32_e32 v7, v7, v18
	v_cvt_i32_f32_e32 v19, v19
	v_add_f32_e32 v8, v8, v20
	v_fmac_f32_e32 v9, 0xb2a5705f, v14
	v_sub_f32_e32 v18, v22, v23
	v_exp_f32_e32 v7, v7
	v_cvt_i32_f32_e32 v16, v16
	v_cvt_i32_f32_e32 v21, v21
	v_exp_f32_e32 v6, v6
	v_exp_f32_e32 v8, v8
	v_add_f32_e32 v9, v18, v9
	v_cvt_i32_f32_e32 v20, v23
	v_exp_f32_e32 v9, v9
	v_ldexp_f32 v7, v7, v19
	v_cmp_nlt_f32_e64 s[2:3], s33, v10
	v_ldexp_f32 v6, v6, v16
	v_cmp_nlt_f32_e32 vcc, s33, v17
	v_ldexp_f32 v8, v8, v21
	v_cndmask_b32_e64 v7, 0, v7, s[2:3]
	v_cmp_ngt_f32_e64 s[2:3], s1, v10
	v_cmp_nlt_f32_e64 s[4:5], s33, v11
	v_cndmask_b32_e32 v6, 0, v6, vcc
	v_cmp_ngt_f32_e32 vcc, s1, v17
	v_cndmask_b32_e64 v8, 0, v8, s[4:5]
	v_ldexp_f32 v16, v9, v20
	v_cndmask_b32_e64 v9, v152, v7, s[2:3]
	v_cmp_ngt_f32_e64 s[2:3], s1, v11
	v_cndmask_b32_e32 v6, v152, v6, vcc
	v_cmp_nlt_f32_e32 vcc, s33, v14
	v_cndmask_b32_e64 v7, v152, v8, s[2:3]
	v_pk_add_f32 v[6:7], v[6:7], 1.0 op_sel_hi:[1,0]
	v_cndmask_b32_e32 v8, 0, v16, vcc
	v_cmp_ngt_f32_e32 vcc, s1, v14
	v_div_scale_f32 v16, s[2:3], v7, v7, v11
	s_nop 0
	v_cndmask_b32_e32 v8, v152, v8, vcc
	v_div_scale_f32 v19, s[2:3], v6, v6, v17
	v_pk_add_f32 v[8:9], v[8:9], 1.0 op_sel_hi:[1,0]
	v_rcp_f32_e32 v21, v16
	v_rcp_f32_e32 v22, v19
	v_div_scale_f32 v23, s[4:5], v9, v9, v10
	v_div_scale_f32 v25, s[6:7], v8, v8, v14
	v_rcp_f32_e32 v27, v23
	v_rcp_f32_e32 v28, v25
	v_fma_f32 v29, -v16, v21, 1.0
	v_div_scale_f32 v18, vcc, v11, v7, v11
	v_fma_f32 v30, -v19, v22, 1.0
	v_fmac_f32_e32 v21, v29, v21
	v_div_scale_f32 v20, s[2:3], v17, v6, v17
	v_fmac_f32_e32 v22, v30, v22
	v_fma_f32 v29, -v23, v27, 1.0
	v_mul_f32_e32 v31, v18, v21
	v_div_scale_f32 v24, s[4:5], v10, v9, v10
	v_fma_f32 v30, -v25, v28, 1.0
	v_mul_f32_e32 v32, v20, v22
	v_fmac_f32_e32 v27, v29, v27
	v_fma_f32 v29, -v16, v31, v18
	v_div_scale_f32 v26, s[6:7], v14, v8, v14
	v_fmac_f32_e32 v28, v30, v28
	v_fma_f32 v30, -v19, v32, v20
	v_mul_f32_e32 v33, v24, v27
	v_fmac_f32_e32 v31, v29, v21
	v_mul_f32_e32 v34, v26, v28
	v_fmac_f32_e32 v32, v30, v22
	v_fma_f32 v29, -v23, v33, v24
	v_fma_f32 v16, -v16, v31, v18
	v_fma_f32 v30, -v25, v34, v26
	v_fma_f32 v18, -v19, v32, v20
	v_fmac_f32_e32 v33, v29, v27
	v_div_fmas_f32 v16, v16, v21, v31
	s_mov_b64 vcc, s[2:3]
	v_fmac_f32_e32 v34, v30, v28
	v_fma_f32 v19, -v23, v33, v24
	v_div_fixup_f32 v7, v16, v7, v11
	v_div_fmas_f32 v11, v18, v22, v32
	s_mov_b64 vcc, s[4:5]
	v_fma_f32 v20, -v25, v34, v26
	v_div_fixup_f32 v6, v11, v6, v17
	v_div_fmas_f32 v11, v19, v27, v33
	s_mov_b64 vcc, s[6:7]
	ds_write_b32 v13, v6
	ds_write_b32 v5, v7
	v_div_fmas_f32 v6, v20, v28, v34
	v_div_fixup_f32 v6, v6, v8, v14
	v_div_fixup_f32 v5, v11, v9, v10
	ds_write_b32 v15, v6
	ds_write_b32 v12, v5
	v_mov_b32_e32 v34, v2
	v_lshlrev_b32_e32 v10, 3, v2
	v_lshrrev_b32_e32 v11, 9, v2
	v_add_u32_e32 v6, 0x400, v3
	v_mov_b32_e32 v7, v35
	s_waitcnt lgkmcnt(0)
	v_lshl_add_u64 v[8:9], v[34:35], 2, s[14:15]
	v_mov_b32_e32 v34, v3
	v_and_b32_e32 v13, 0x3ff8, v10
	v_and_b32_e32 v14, 0x7ffffc, v11
	v_lshl_add_u64 v[10:11], v[6:7], 2, s[14:15]
	v_lshlrev_b32_e32 v15, 3, v6
	v_lshrrev_b32_e32 v16, 9, v6
	v_lshl_add_u64 v[6:7], v[34:35], 2, s[14:15]
	v_add_u32_e32 v34, 0x400, v2
	v_lshlrev_b32_e32 v13, 2, v13
	s_nop 0
	s_nop 0
	v_lshl_add_u64 v[6:7], v[34:35], 2, s[14:15]
	v_add3_u32 v13, 0, v13, v14
	v_lshlrev_b32_e32 v5, 3, v3
	v_lshrrev_b32_e32 v12, 9, v3
	v_and_b32_e32 v5, 0x3ff8, v5
	v_and_b32_e32 v12, 0x7ffffc, v12
	v_lshlrev_b32_e32 v5, 2, v5
	v_lshlrev_b32_e32 v8, 3, v34
	v_add3_u32 v5, 0, v5, v12
	v_lshrrev_b32_e32 v12, 9, v34
	v_and_b32_e32 v6, 0x3ff8, v8
	v_and_b32_e32 v15, 0x3ff8, v15
	v_and_b32_e32 v7, 0x7ffffc, v12
	v_lshlrev_b32_e32 v6, 2, v6
	v_and_b32_e32 v16, 0x7ffffc, v16
	v_lshlrev_b32_e32 v9, 2, v15
	v_add3_u32 v15, 0, v6, v7
	v_add3_u32 v12, 0, v9, v16
	v_add_u32_e32 v4, -2, v4
	v_cmp_eq_u32_e32 vcc, 0, v4
	s_or_b64 s[8:9], vcc, s[8:9]
	v_add_u32_e32 v3, 0x800, v3
	v_add_u32_e32 v2, 0x800, v2
	s_waitcnt vmcnt(4)
; __device__ __forceinline__ void ph0_adaln(const Args& a, LAS unsigned char* lds, int tid, int G, int bid) {
;     ...
;     for (int ub = bid; ub < MODW / 64; ub += G) {
;         if (!have) { for (int i = tid; i < NB * DM; i += NTHR) { const int b = i >> 11, k = i & 2047; const float v = c[i]; cond[k * 8 + b] = v / (1.0f + expf(-v)); } __syncthreads(); have = true; }
	v_mov_b32_e32 v17, v70
	v_mov_b32_e32 v10, v71
	v_mov_b32_e32 v11, v72
	v_mov_b32_e32 v14, v73
	v_mul_f32_e32 v6, 0xbfb8aa3b, v17
	v_mul_f32_e32 v7, 0xbfb8aa3b, v10
	v_mul_f32_e32 v8, 0xbfb8aa3b, v11
	v_fma_f32 v9, v17, s10, -v6
	v_rndne_f32_e32 v16, v6
	v_fma_f32 v18, v10, s10, -v7
	v_rndne_f32_e32 v19, v7
	v_fma_f32 v20, v11, s10, -v8
	v_rndne_f32_e32 v21, v8
	v_fmac_f32_e32 v9, 0xb2a5705f, v17
	v_sub_f32_e32 v6, v6, v16
	v_mul_f32_e32 v22, 0xbfb8aa3b, v14
	v_fmac_f32_e32 v18, 0xb2a5705f, v10
	v_sub_f32_e32 v7, v7, v19
	v_fmac_f32_e32 v20, 0xb2a5705f, v11
	v_sub_f32_e32 v8, v8, v21
	v_add_f32_e32 v6, v6, v9
	v_fma_f32 v9, v14, s10, -v22
	v_rndne_f32_e32 v23, v22
	v_add_f32_e32 v7, v7, v18
	v_cvt_i32_f32_e32 v19, v19
	v_add_f32_e32 v8, v8, v20
	v_fmac_f32_e32 v9, 0xb2a5705f, v14
	v_sub_f32_e32 v18, v22, v23
	v_exp_f32_e32 v7, v7
	v_cvt_i32_f32_e32 v16, v16
	v_cvt_i32_f32_e32 v21, v21
	v_exp_f32_e32 v6, v6
	v_exp_f32_e32 v8, v8
	v_add_f32_e32 v9, v18, v9
	v_cvt_i32_f32_e32 v20, v23
	v_exp_f32_e32 v9, v9
	v_ldexp_f32 v7, v7, v19
	v_cmp_nlt_f32_e64 s[2:3], s33, v10
	v_ldexp_f32 v6, v6, v16
	v_cmp_nlt_f32_e32 vcc, s33, v17
	v_ldexp_f32 v8, v8, v21
	v_cndmask_b32_e64 v7, 0, v7, s[2:3]
	v_cmp_ngt_f32_e64 s[2:3], s1, v10
	v_cmp_nlt_f32_e64 s[4:5], s33, v11
	v_cndmask_b32_e32 v6, 0, v6, vcc
	v_cmp_ngt_f32_e32 vcc, s1, v17
	v_cndmask_b32_e64 v8, 0, v8, s[4:5]
	v_ldexp_f32 v16, v9, v20
	v_cndmask_b32_e64 v9, v152, v7, s[2:3]
	v_cmp_ngt_f32_e64 s[2:3], s1, v11
	v_cndmask_b32_e32 v6, v152, v6, vcc
	v_cmp_nlt_f32_e32 vcc, s33, v14
	v_cndmask_b32_e64 v7, v152, v8, s[2:3]
	v_pk_add_f32 v[6:7], v[6:7], 1.0 op_sel_hi:[1,0]
	v_cndmask_b32_e32 v8, 0, v16, vcc
	v_cmp_ngt_f32_e32 vcc, s1, v14
	v_div_scale_f32 v16, s[2:3], v7, v7, v11
	s_nop 0
	v_cndmask_b32_e32 v8, v152, v8, vcc
	v_div_scale_f32 v19, s[2:3], v6, v6, v17
	v_pk_add_f32 v[8:9], v[8:9], 1.0 op_sel_hi:[1,0]
	v_rcp_f32_e32 v21, v16
	v_rcp_f32_e32 v22, v19
	v_div_scale_f32 v23, s[4:5], v9, v9, v10
	v_div_scale_f32 v25, s[6:7], v8, v8, v14
	v_rcp_f32_e32 v27, v23
	v_rcp_f32_e32 v28, v25
	v_fma_f32 v29, -v16, v21, 1.0
	v_div_scale_f32 v18, vcc, v11, v7, v11
	v_fma_f32 v30, -v19, v22, 1.0
	v_fmac_f32_e32 v21, v29, v21
	v_div_scale_f32 v20, s[2:3], v17, v6, v17
	v_fmac_f32_e32 v22, v30, v22
	v_fma_f32 v29, -v23, v27, 1.0
	v_mul_f32_e32 v31, v18, v21
	v_div_scale_f32 v24, s[4:5], v10, v9, v10
	v_fma_f32 v30, -v25, v28, 1.0
	v_mul_f32_e32 v32, v20, v22
	v_fmac_f32_e32 v27, v29, v27
	v_fma_f32 v29, -v16, v31, v18
	v_div_scale_f32 v26, s[6:7], v14, v8, v14
	v_fmac_f32_e32 v28, v30, v28
	v_fma_f32 v30, -v19, v32, v20
	v_mul_f32_e32 v33, v24, v27
	v_fmac_f32_e32 v31, v29, v21
	v_mul_f32_e32 v34, v26, v28
	v_fmac_f32_e32 v32, v30, v22
	v_fma_f32 v29, -v23, v33, v24
	v_fma_f32 v16, -v16, v31, v18
	v_fma_f32 v30, -v25, v34, v26
	v_fma_f32 v18, -v19, v32, v20
	v_fmac_f32_e32 v33, v29, v27
	v_div_fmas_f32 v16, v16, v21, v31
	s_mov_b64 vcc, s[2:3]
	v_fmac_f32_e32 v34, v30, v28
	v_fma_f32 v19, -v23, v33, v24
	v_div_fixup_f32 v7, v16, v7, v11
	v_div_fmas_f32 v11, v18, v22, v32
	s_mov_b64 vcc, s[4:5]
	v_fma_f32 v20, -v25, v34, v26
	v_div_fixup_f32 v6, v11, v6, v17
	v_div_fmas_f32 v11, v19, v27, v33
	s_mov_b64 vcc, s[6:7]
	ds_write_b32 v13, v6
	ds_write_b32 v5, v7
	v_div_fmas_f32 v6, v20, v28, v34
	v_div_fixup_f32 v6, v6, v8, v14
	v_div_fixup_f32 v5, v11, v9, v10
	ds_write_b32 v15, v6
	ds_write_b32 v12, v5
	v_mov_b32_e32 v34, v2
	v_lshlrev_b32_e32 v10, 3, v2
	v_lshrrev_b32_e32 v11, 9, v2
	v_add_u32_e32 v6, 0x400, v3
	v_mov_b32_e32 v7, v35
	s_waitcnt lgkmcnt(0)
	v_lshl_add_u64 v[8:9], v[34:35], 2, s[14:15]
	v_mov_b32_e32 v34, v3
	v_and_b32_e32 v13, 0x3ff8, v10
	v_and_b32_e32 v14, 0x7ffffc, v11
	v_lshl_add_u64 v[10:11], v[6:7], 2, s[14:15]
	v_lshlrev_b32_e32 v15, 3, v6
	v_lshrrev_b32_e32 v16, 9, v6
	v_lshl_add_u64 v[6:7], v[34:35], 2, s[14:15]
	v_add_u32_e32 v34, 0x400, v2
	v_lshlrev_b32_e32 v13, 2, v13
	s_nop 0
	s_nop 0
	v_lshl_add_u64 v[6:7], v[34:35], 2, s[14:15]
	v_add3_u32 v13, 0, v13, v14
	v_lshlrev_b32_e32 v5, 3, v3
	v_lshrrev_b32_e32 v12, 9, v3
	v_and_b32_e32 v5, 0x3ff8, v5
	v_and_b32_e32 v12, 0x7ffffc, v12
	v_lshlrev_b32_e32 v5, 2, v5
	v_lshlrev_b32_e32 v8, 3, v34
	v_add3_u32 v5, 0, v5, v12
	v_lshrrev_b32_e32 v12, 9, v34
	v_and_b32_e32 v6, 0x3ff8, v8
	v_and_b32_e32 v15, 0x3ff8, v15
	v_and_b32_e32 v7, 0x7ffffc, v12
	v_lshlrev_b32_e32 v6, 2, v6
	v_and_b32_e32 v16, 0x7ffffc, v16
	v_lshlrev_b32_e32 v9, 2, v15
	v_add3_u32 v15, 0, v6, v7
	v_add3_u32 v12, 0, v9, v16
	v_add_u32_e32 v4, -2, v4
	v_cmp_eq_u32_e32 vcc, 0, v4
	s_or_b64 s[8:9], vcc, s[8:9]
	v_add_u32_e32 v3, 0x800, v3
	v_add_u32_e32 v2, 0x800, v2
	s_waitcnt vmcnt(0)
; __device__ __forceinline__ void ph0_adaln(const Args& a, LAS unsigned char* lds, int tid, int G, int bid) {
;     ...
;     for (int ub = bid; ub < MODW / 64; ub += G) {
;         if (!have) { for (int i = tid; i < NB * DM; i += NTHR) { const int b = i >> 11, k = i & 2047; const float v = c[i]; cond[k * 8 + b] = v / (1.0f + expf(-v)); } __syncthreads(); have = true; }
	v_mov_b32_e32 v17, v74
	v_mov_b32_e32 v10, v75
	v_mov_b32_e32 v11, v76
	v_mov_b32_e32 v14, v77
	v_mul_f32_e32 v6, 0xbfb8aa3b, v17
	v_mul_f32_e32 v7, 0xbfb8aa3b, v10
	v_mul_f32_e32 v8, 0xbfb8aa3b, v11
	v_fma_f32 v9, v17, s10, -v6
	v_rndne_f32_e32 v16, v6
	v_fma_f32 v18, v10, s10, -v7
	v_rndne_f32_e32 v19, v7
	v_fma_f32 v20, v11, s10, -v8
	v_rndne_f32_e32 v21, v8
	v_fmac_f32_e32 v9, 0xb2a5705f, v17
	v_sub_f32_e32 v6, v6, v16
	v_mul_f32_e32 v22, 0xbfb8aa3b, v14
	v_fmac_f32_e32 v18, 0xb2a5705f, v10
	v_sub_f32_e32 v7, v7, v19
	v_fmac_f32_e32 v20, 0xb2a5705f, v11
	v_sub_f32_e32 v8, v8, v21
	v_add_f32_e32 v6, v6, v9
	v_fma_f32 v9, v14, s10, -v22
	v_rndne_f32_e32 v23, v22
	v_add_f32_e32 v7, v7, v18
	v_cvt_i32_f32_e32 v19, v19
	v_add_f32_e32 v8, v8, v20
	v_fmac_f32_e32 v9, 0xb2a5705f, v14
	v_sub_f32_e32 v18, v22, v23
	v_exp_f32_e32 v7, v7
	v_cvt_i32_f32_e32 v16, v16
	v_cvt_i32_f32_e32 v21, v21
	v_exp_f32_e32 v6, v6
	v_exp_f32_e32 v8, v8
	v_add_f32_e32 v9, v18, v9
	v_cvt_i32_f32_e32 v20, v23
	v_exp_f32_e32 v9, v9
	v_ldexp_f32 v7, v7, v19
	v_cmp_nlt_f32_e64 s[2:3], s33, v10
	v_ldexp_f32 v6, v6, v16
	v_cmp_nlt_f32_e32 vcc, s33, v17
	v_ldexp_f32 v8, v8, v21
	v_cndmask_b32_e64 v7, 0, v7, s[2:3]
	v_cmp_ngt_f32_e64 s[2:3], s1, v10
	v_cmp_nlt_f32_e64 s[4:5], s33, v11
	v_cndmask_b32_e32 v6, 0, v6, vcc
	v_cmp_ngt_f32_e32 vcc, s1, v17
	v_cndmask_b32_e64 v8, 0, v8, s[4:5]
	v_ldexp_f32 v16, v9, v20
	v_cndmask_b32_e64 v9, v152, v7, s[2:3]
	v_cmp_ngt_f32_e64 s[2:3], s1, v11
	v_cndmask_b32_e32 v6, v152, v6, vcc
	v_cmp_nlt_f32_e32 vcc, s33, v14
	v_cndmask_b32_e64 v7, v152, v8, s[2:3]
	v_pk_add_f32 v[6:7], v[6:7], 1.0 op_sel_hi:[1,0]
	v_cndmask_b32_e32 v8, 0, v16, vcc
	v_cmp_ngt_f32_e32 vcc, s1, v14
	v_div_scale_f32 v16, s[2:3], v7, v7, v11
	s_nop 0
	v_cndmask_b32_e32 v8, v152, v8, vcc
	v_div_scale_f32 v19, s[2:3], v6, v6, v17
	v_pk_add_f32 v[8:9], v[8:9], 1.0 op_sel_hi:[1,0]
	v_rcp_f32_e32 v21, v16
	v_rcp_f32_e32 v22, v19
	v_div_scale_f32 v23, s[4:5], v9, v9, v10
	v_div_scale_f32 v25, s[6:7], v8, v8, v14
	v_rcp_f32_e32 v27, v23
	v_rcp_f32_e32 v28, v25
	v_fma_f32 v29, -v16, v21, 1.0
	v_div_scale_f32 v18, vcc, v11, v7, v11
	v_fma_f32 v30, -v19, v22, 1.0
	v_fmac_f32_e32 v21, v29, v21
	v_div_scale_f32 v20, s[2:3], v17, v6, v17
	v_fmac_f32_e32 v22, v30, v22
	v_fma_f32 v29, -v23, v27, 1.0
	v_mul_f32_e32 v31, v18, v21
	v_div_scale_f32 v24, s[4:5], v10, v9, v10
	v_fma_f32 v30, -v25, v28, 1.0
	v_mul_f32_e32 v32, v20, v22
	v_fmac_f32_e32 v27, v29, v27
	v_fma_f32 v29, -v16, v31, v18
	v_div_scale_f32 v26, s[6:7], v14, v8, v14
	v_fmac_f32_e32 v28, v30, v28
	v_fma_f32 v30, -v19, v32, v20
	v_mul_f32_e32 v33, v24, v27
	v_fmac_f32_e32 v31, v29, v21
	v_mul_f32_e32 v34, v26, v28
	v_fmac_f32_e32 v32, v30, v22
	v_fma_f32 v29, -v23, v33, v24
	v_fma_f32 v16, -v16, v31, v18
	v_fma_f32 v30, -v25, v34, v26
	v_fma_f32 v18, -v19, v32, v20
	v_fmac_f32_e32 v33, v29, v27
	v_div_fmas_f32 v16, v16, v21, v31
	s_mov_b64 vcc, s[2:3]
	v_fmac_f32_e32 v34, v30, v28
	v_fma_f32 v19, -v23, v33, v24
	v_div_fixup_f32 v7, v16, v7, v11
	v_div_fmas_f32 v11, v18, v22, v32
	s_mov_b64 vcc, s[4:5]
	v_fma_f32 v20, -v25, v34, v26
	v_div_fixup_f32 v6, v11, v6, v17
	v_div_fmas_f32 v11, v19, v27, v33
	s_mov_b64 vcc, s[6:7]
	ds_write_b32 v13, v6
	ds_write_b32 v5, v7
	v_div_fmas_f32 v6, v20, v28, v34
	v_div_fixup_f32 v6, v6, v8, v14
	v_div_fixup_f32 v5, v11, v9, v10
	ds_write_b32 v15, v6
	ds_write_b32 v12, v5
	s_or_b64 exec, exec, s[8:9]
	s_mov_b64 s[4:5], exec
	s_mov_b64 s[2:3], 0
	s_and_b64 s[2:3], s[4:5], s[2:3]
	s_mov_b64 exec, s[2:3]
	s_cbranch_execz .LBB0_28
	v_mov_b32_e32 v34, v2
	v_lshl_add_u64 v[4:5], v[34:35], 2, s[14:15]
	v_mov_b32_e32 v34, v3
	v_lshl_add_u64 v[6:7], v[34:35], 2, s[14:15]
	global_load_dword v4, v[4:5], off
	s_nop 0
	global_load_dword v5, v[6:7], off
	v_lshlrev_b32_e32 v7, 3, v2
	v_lshlrev_b32_e32 v6, 3, v3
	v_lshrrev_b32_e32 v2, 9, v2
	v_and_b32_e32 v7, 0x3ff8, v7
	v_lshrrev_b32_e32 v3, 9, v3
	v_and_b32_e32 v6, 0x3ff8, v6
	v_and_b32_e32 v2, 0x7ffffc, v2
	v_lshlrev_b32_e32 v7, 2, v7
	v_and_b32_e32 v3, 0x7ffffc, v3
	v_lshlrev_b32_e32 v6, 2, v6
	v_add3_u32 v7, 0, v7, v2
	v_add3_u32 v6, 0, v6, v3
	s_waitcnt vmcnt(1)
	v_mul_f32_e32 v8, 0xbfb8aa3b, v4
	s_waitcnt vmcnt(0)
	v_mul_f32_e32 v9, 0xbfb8aa3b, v5
	v_fma_f32 v10, v4, s10, -v8
	v_rndne_f32_e32 v11, v8
	v_fma_f32 v12, v5, s10, -v9
	v_rndne_f32_e32 v13, v9
	v_fmac_f32_e32 v10, 0xb2a5705f, v4
	v_sub_f32_e32 v8, v8, v11
	v_fmac_f32_e32 v12, 0xb2a5705f, v5
	v_sub_f32_e32 v9, v9, v13
	v_add_f32_e32 v8, v8, v10
	v_cvt_i32_f32_e32 v11, v11
	v_add_f32_e32 v9, v9, v12
	v_exp_f32_e32 v8, v8
	v_cvt_i32_f32_e32 v13, v13
	v_exp_f32_e32 v9, v9
	v_cmp_nlt_f32_e32 vcc, s33, v4
	v_ldexp_f32 v2, v8, v11
	v_ldexp_f32 v3, v9, v13
	v_cndmask_b32_e32 v2, 0, v2, vcc
	v_cmp_nlt_f32_e32 vcc, s33, v5
	s_nop 1
	v_cndmask_b32_e32 v3, 0, v3, vcc
	v_cmp_ngt_f32_e32 vcc, s1, v4
	s_nop 1
	v_cndmask_b32_e32 v2, v152, v2, vcc
	v_cmp_ngt_f32_e32 vcc, s1, v5
	s_nop 1
	v_cndmask_b32_e32 v3, v152, v3, vcc
	v_pk_add_f32 v[2:3], v[2:3], 1.0 op_sel_hi:[1,0]
	s_nop 0
	v_div_scale_f32 v8, s[2:3], v3, v3, v5
	v_div_scale_f32 v10, s[2:3], v2, v2, v4
	v_rcp_f32_e32 v11, v8
	v_rcp_f32_e32 v12, v10
	v_div_scale_f32 v9, vcc, v5, v3, v5
	v_fma_f32 v14, -v8, v11, 1.0
	v_fma_f32 v15, -v10, v12, 1.0
	v_fmac_f32_e32 v11, v14, v11
	v_div_scale_f32 v13, s[2:3], v4, v2, v4
	v_fmac_f32_e32 v12, v15, v12
	v_mul_f32_e32 v14, v9, v11
	v_mul_f32_e32 v15, v13, v12
	v_fma_f32 v16, -v8, v14, v9
	v_fma_f32 v17, -v10, v15, v13
	v_fmac_f32_e32 v14, v16, v11
	v_fmac_f32_e32 v15, v17, v12
	v_fma_f32 v8, -v8, v14, v9
	v_fma_f32 v9, -v10, v15, v13
	v_div_fmas_f32 v8, v8, v11, v14
	s_mov_b64 vcc, s[2:3]
	v_div_fixup_f32 v3, v8, v3, v5
	v_div_fmas_f32 v5, v9, v12, v15
	v_div_fixup_f32 v2, v5, v2, v4
	ds_write_b32 v7, v2
	ds_write_b32 v6, v3
